# v55 + the swiglu epilogue's h stores (dwordx4) issued with sc1: written through, not retained in the XCD L2 (h is 11.5 MB per XCD and is read back only in the next phase)
# speedup vs baseline: 1.0236x; 1.0236x over previous
; #define PG8_LAS __attribute__((address_space(3)))
; __device__ __forceinline__ u32x4 pack8(const f32x4 a, const f32x4 b) { u32x4 w; w.x = cvt_pk_bf16(a[0], a[1]); w.y = cvt_pk_bf16(a[2], a[3]); w.z = cvt_pk_bf16(b[0], b[1]); w.w = cvt_pk_bf16(b[2], b[3]); return w; }
; __device__ __forceinline__ float sigm(float x) { return __builtin_amdgcn_rcpf(1.0f + __builtin_amdgcn_exp2f(-1.4426950408889634f * x)); }
;     __device__ __forceinline__ void operator()(const f32x4 (&acc)[2][2][4][2], const Unit& u, int wr, int wc, int fr, int fq) const {
;         const int rl0 = wr * 64 + fr + (u.half == 2 ? HALF : 0), row0 = u.pm * BM + rl0, col0 = u.pn * HALF + wc * 32 + 8 * fq; const PG8_LAS float* rsr = rsl + rl0;
; #pragma unroll
;         for (int ai = 0; ai < 2; ++ai) { if (ai == 1 && u.half != 0) break;
; #pragma unroll
;             for (int m = 0; m < 4; ++m) { const float rf = rsr[ai * HALF + m * 16]; f32x4 v0 = acc[ai][0][m][0] * rf, v1 = acc[ai][0][m][1] * rf; const f32x4 u0 = acc[ai][1][m][0] * rf, u1 = acc[ai][1][m][1] * rf;
; #pragma unroll
;                 for (int e = 0; e < 4; ++e) { v0[e] = v0[e] * sigm(v0[e]) * u0[e]; v1[e] = v1[e] * sigm(v1[e]) * u1[e]; }
;                 *(u32x4*)(H + (size_t)(row0 + ai * HALF + m * 16) * DFF + col0) = pack8(v0, v1); } }
.LBB0_1480:
	ds_read_b32 v236, v148
	ds_read_b32 v237, v148 offset:64
	ds_read_b32 v238, v148 offset:128
	ds_read_b32 v239, v148 offset:192
	ds_read_b32 v240, v148 offset:512
	ds_read_b32 v241, v148 offset:576
	ds_read_b32 v242, v148 offset:640
	ds_read_b32 v243, v148 offset:704
	v_lshl_or_b32 v252, s20, 7, v149
	v_lshl_add_u32 v253, s14, 8, v146
	v_lshlrev_b32_e32 v252, 1, v252
	v_mad_u32_u24 v252, v253, s2, v252
	s_mov_b32 s0, 0xbfb8aa3b
	s_waitcnt lgkmcnt(0)
	v_pk_mul_f32 v[244:245], v[236:237], s[0:1] op_sel_hi:[1,0]
	v_pk_mul_f32 v[246:247], v[238:239], s[0:1] op_sel_hi:[1,0]
	v_pk_mul_f32 v[248:249], v[240:241], s[0:1] op_sel_hi:[1,0]
	v_pk_mul_f32 v[250:251], v[242:243], s[0:1] op_sel_hi:[1,0]
	v_pk_mul_f32 v[236:237], v[236:237], v[236:237]
	v_pk_mul_f32 v[238:239], v[238:239], v[238:239]
	v_pk_mul_f32 v[240:241], v[240:241], v[240:241]
	v_pk_mul_f32 v[242:243], v[242:243], v[242:243]
	v_rcp_f32_e32 v236, v236
	v_rcp_f32_e32 v237, v237
	v_rcp_f32_e32 v238, v238
	v_rcp_f32_e32 v239, v239
	v_rcp_f32_e32 v240, v240
	v_rcp_f32_e32 v241, v241
	v_rcp_f32_e32 v242, v242
	v_rcp_f32_e32 v243, v243
	v_pk_mul_f32 v[228:229], v[128:129], v[244:245] op_sel:[0,0] op_sel_hi:[1,0]
	v_pk_mul_f32 v[230:231], v[130:131], v[244:245] op_sel:[0,0] op_sel_hi:[1,0]
	v_pk_mul_f32 v[232:233], v[124:125], v[244:245] op_sel:[0,0] op_sel_hi:[1,0]
	v_pk_mul_f32 v[234:235], v[126:127], v[244:245] op_sel:[0,0] op_sel_hi:[1,0]
	v_exp_f32_e32 v228, v228
	v_exp_f32_e32 v229, v229
	v_exp_f32_e32 v230, v230
	v_exp_f32_e32 v231, v231
	v_exp_f32_e32 v232, v232
	v_exp_f32_e32 v233, v233
	v_exp_f32_e32 v234, v234
	v_exp_f32_e32 v235, v235
	v_pk_fma_f32 v[228:229], v[228:229], v[236:237], v[236:237] op_sel:[0,0,0] op_sel_hi:[1,0,0]
	v_pk_fma_f32 v[230:231], v[230:231], v[236:237], v[236:237] op_sel:[0,0,0] op_sel_hi:[1,0,0]
	v_pk_fma_f32 v[232:233], v[232:233], v[236:237], v[236:237] op_sel:[0,0,0] op_sel_hi:[1,0,0]
	v_pk_fma_f32 v[234:235], v[234:235], v[236:237], v[236:237] op_sel:[0,0,0] op_sel_hi:[1,0,0]
	v_rcp_f32_e32 v228, v228
	v_rcp_f32_e32 v229, v229
	v_rcp_f32_e32 v230, v230
	v_rcp_f32_e32 v231, v231
	v_rcp_f32_e32 v232, v232
	v_rcp_f32_e32 v233, v233
	v_rcp_f32_e32 v234, v234
	v_rcp_f32_e32 v235, v235
	v_pk_mul_f32 v[120:121], v[128:129], v[120:121]
	v_pk_mul_f32 v[122:123], v[130:131], v[122:123]
	v_pk_mul_f32 v[116:117], v[124:125], v[116:117]
	v_pk_mul_f32 v[118:119], v[126:127], v[118:119]
	v_pk_mul_f32 v[128:129], v[120:121], v[228:229]
	v_pk_mul_f32 v[130:131], v[122:123], v[230:231]
	v_pk_mul_f32 v[124:125], v[116:117], v[232:233]
	v_pk_mul_f32 v[126:127], v[118:119], v[234:235]
	v_cvt_pk_bf16_f32 v128, v128, v129
	v_cvt_pk_bf16_f32 v129, v130, v131
	v_cvt_pk_bf16_f32 v130, v124, v125
	v_cvt_pk_bf16_f32 v131, v126, v127
	global_store_dwordx4 v252, v[128:131], s[4:5] sc1
	v_pk_mul_f32 v[228:229], v[112:113], v[244:245] op_sel:[0,1] op_sel_hi:[1,1]
	v_pk_mul_f32 v[230:231], v[114:115], v[244:245] op_sel:[0,1] op_sel_hi:[1,1]
	v_pk_mul_f32 v[232:233], v[108:109], v[244:245] op_sel:[0,1] op_sel_hi:[1,1]
	v_pk_mul_f32 v[234:235], v[110:111], v[244:245] op_sel:[0,1] op_sel_hi:[1,1]
	v_exp_f32_e32 v228, v228
	v_exp_f32_e32 v229, v229
	v_exp_f32_e32 v230, v230
	v_exp_f32_e32 v231, v231
	v_exp_f32_e32 v232, v232
	v_exp_f32_e32 v233, v233
	v_exp_f32_e32 v234, v234
	v_exp_f32_e32 v235, v235
	v_pk_fma_f32 v[228:229], v[228:229], v[236:237], v[236:237] op_sel:[0,1,1] op_sel_hi:[1,1,1]
	v_pk_fma_f32 v[230:231], v[230:231], v[236:237], v[236:237] op_sel:[0,1,1] op_sel_hi:[1,1,1]
	v_pk_fma_f32 v[232:233], v[232:233], v[236:237], v[236:237] op_sel:[0,1,1] op_sel_hi:[1,1,1]
	v_pk_fma_f32 v[234:235], v[234:235], v[236:237], v[236:237] op_sel:[0,1,1] op_sel_hi:[1,1,1]
	v_rcp_f32_e32 v228, v228
	v_rcp_f32_e32 v229, v229
	v_rcp_f32_e32 v230, v230
	v_rcp_f32_e32 v231, v231
	v_rcp_f32_e32 v232, v232
	v_rcp_f32_e32 v233, v233
	v_rcp_f32_e32 v234, v234
	v_rcp_f32_e32 v235, v235
	v_pk_mul_f32 v[104:105], v[112:113], v[104:105]
	v_pk_mul_f32 v[106:107], v[114:115], v[106:107]
	v_pk_mul_f32 v[100:101], v[108:109], v[100:101]
	v_pk_mul_f32 v[102:103], v[110:111], v[102:103]
	v_add_u32_e32 v252, 0x16000, v252
	v_pk_mul_f32 v[112:113], v[104:105], v[228:229]
	v_pk_mul_f32 v[114:115], v[106:107], v[230:231]
	v_pk_mul_f32 v[108:109], v[100:101], v[232:233]
	v_pk_mul_f32 v[110:111], v[102:103], v[234:235]
	v_cvt_pk_bf16_f32 v104, v112, v113
	v_cvt_pk_bf16_f32 v105, v114, v115
	v_cvt_pk_bf16_f32 v106, v108, v109
	v_cvt_pk_bf16_f32 v107, v110, v111
	global_store_dwordx4 v252, v[104:107], s[4:5] sc1
	v_pk_mul_f32 v[228:229], v[96:97], v[246:247] op_sel:[0,0] op_sel_hi:[1,0]
	v_pk_mul_f32 v[230:231], v[98:99], v[246:247] op_sel:[0,0] op_sel_hi:[1,0]
	v_pk_mul_f32 v[232:233], v[92:93], v[246:247] op_sel:[0,0] op_sel_hi:[1,0]
	v_pk_mul_f32 v[234:235], v[94:95], v[246:247] op_sel:[0,0] op_sel_hi:[1,0]
	v_exp_f32_e32 v228, v228
	v_exp_f32_e32 v229, v229
	v_exp_f32_e32 v230, v230
	v_exp_f32_e32 v231, v231
	v_exp_f32_e32 v232, v232
	v_exp_f32_e32 v233, v233
	v_exp_f32_e32 v234, v234
	v_exp_f32_e32 v235, v235
	v_pk_fma_f32 v[228:229], v[228:229], v[238:239], v[238:239] op_sel:[0,0,0] op_sel_hi:[1,0,0]
	v_pk_fma_f32 v[230:231], v[230:231], v[238:239], v[238:239] op_sel:[0,0,0] op_sel_hi:[1,0,0]
	v_pk_fma_f32 v[232:233], v[232:233], v[238:239], v[238:239] op_sel:[0,0,0] op_sel_hi:[1,0,0]
	v_pk_fma_f32 v[234:235], v[234:235], v[238:239], v[238:239] op_sel:[0,0,0] op_sel_hi:[1,0,0]
	v_rcp_f32_e32 v228, v228
	v_rcp_f32_e32 v229, v229
	v_rcp_f32_e32 v230, v230
	v_rcp_f32_e32 v231, v231
	v_rcp_f32_e32 v232, v232
	v_rcp_f32_e32 v233, v233
	v_rcp_f32_e32 v234, v234
	v_rcp_f32_e32 v235, v235
; __device__ __forceinline__ float sigm(float x) { return __builtin_amdgcn_rcpf(1.0f + __builtin_amdgcn_exp2f(-1.4426950408889634f * x)); }
; __device__ __forceinline__ u32x4 pack8(const f32x4 a, const f32x4 b) { u32x4 w; w.x = cvt_pk_bf16(a[0], a[1]); w.y = cvt_pk_bf16(a[2], a[3]); w.z = cvt_pk_bf16(b[0], b[1]); w.w = cvt_pk_bf16(b[2], b[3]); return w; }
;     __device__ __forceinline__ void operator()(const f32x4 (&acc)[2][2][4][2], const Unit& u, int wr, int wc, int fr, int fq) const {
;     ...
;         for (int ai = 0; ai < 2; ++ai) { if (ai == 1 && u.half != 0) break;
; #pragma unroll
;             for (int m = 0; m < 4; ++m) { const float rf = rsr[ai * HALF + m * 16]; f32x4 v0 = acc[ai][0][m][0] * rf, v1 = acc[ai][0][m][1] * rf; const f32x4 u0 = acc[ai][1][m][0] * rf, u1 = acc[ai][1][m][1] * rf;
; #pragma unroll
;                 for (int e = 0; e < 4; ++e) { v0[e] = v0[e] * sigm(v0[e]) * u0[e]; v1[e] = v1[e] * sigm(v1[e]) * u1[e]; }
;                 *(u32x4*)(H + (size_t)(row0 + ai * HALF + m * 16) * DFF + col0) = pack8(v0, v1); } }
	v_pk_mul_f32 v[88:89], v[96:97], v[88:89]
	v_pk_mul_f32 v[90:91], v[98:99], v[90:91]
	v_pk_mul_f32 v[84:85], v[92:93], v[84:85]
	v_pk_mul_f32 v[86:87], v[94:95], v[86:87]
	v_add_u32_e32 v252, 0x16000, v252
	v_pk_mul_f32 v[96:97], v[88:89], v[228:229]
	v_pk_mul_f32 v[98:99], v[90:91], v[230:231]
	v_pk_mul_f32 v[92:93], v[84:85], v[232:233]
	v_pk_mul_f32 v[94:95], v[86:87], v[234:235]
	v_cvt_pk_bf16_f32 v96, v96, v97
	v_cvt_pk_bf16_f32 v97, v98, v99
	v_cvt_pk_bf16_f32 v98, v92, v93
	v_cvt_pk_bf16_f32 v99, v94, v95
	global_store_dwordx4 v252, v[96:99], s[4:5] sc1
	v_pk_mul_f32 v[228:229], v[80:81], v[246:247] op_sel:[0,1] op_sel_hi:[1,1]
	v_pk_mul_f32 v[230:231], v[82:83], v[246:247] op_sel:[0,1] op_sel_hi:[1,1]
	v_pk_mul_f32 v[232:233], v[76:77], v[246:247] op_sel:[0,1] op_sel_hi:[1,1]
	v_pk_mul_f32 v[234:235], v[78:79], v[246:247] op_sel:[0,1] op_sel_hi:[1,1]
	v_exp_f32_e32 v228, v228
	v_exp_f32_e32 v229, v229
	v_exp_f32_e32 v230, v230
	v_exp_f32_e32 v231, v231
	v_exp_f32_e32 v232, v232
	v_exp_f32_e32 v233, v233
	v_exp_f32_e32 v234, v234
	v_exp_f32_e32 v235, v235
	v_pk_fma_f32 v[228:229], v[228:229], v[238:239], v[238:239] op_sel:[0,1,1] op_sel_hi:[1,1,1]
	v_pk_fma_f32 v[230:231], v[230:231], v[238:239], v[238:239] op_sel:[0,1,1] op_sel_hi:[1,1,1]
	v_pk_fma_f32 v[232:233], v[232:233], v[238:239], v[238:239] op_sel:[0,1,1] op_sel_hi:[1,1,1]
	v_pk_fma_f32 v[234:235], v[234:235], v[238:239], v[238:239] op_sel:[0,1,1] op_sel_hi:[1,1,1]
	v_rcp_f32_e32 v228, v228
	v_rcp_f32_e32 v229, v229
	v_rcp_f32_e32 v230, v230
	v_rcp_f32_e32 v231, v231
	v_rcp_f32_e32 v232, v232
	v_rcp_f32_e32 v233, v233
	v_rcp_f32_e32 v234, v234
	v_rcp_f32_e32 v235, v235
	v_pk_mul_f32 v[72:73], v[80:81], v[72:73]
	v_pk_mul_f32 v[74:75], v[82:83], v[74:75]
	v_pk_mul_f32 v[68:69], v[76:77], v[68:69]
	v_pk_mul_f32 v[70:71], v[78:79], v[70:71]
	v_add_u32_e32 v252, 0x16000, v252
	v_pk_mul_f32 v[80:81], v[72:73], v[228:229]
	v_pk_mul_f32 v[82:83], v[74:75], v[230:231]
	v_pk_mul_f32 v[76:77], v[68:69], v[232:233]
	v_pk_mul_f32 v[78:79], v[70:71], v[234:235]
	v_cvt_pk_bf16_f32 v72, v80, v81
	v_cvt_pk_bf16_f32 v73, v82, v83
	v_cvt_pk_bf16_f32 v74, v76, v77
	v_cvt_pk_bf16_f32 v75, v78, v79
	global_store_dwordx4 v252, v[72:75], s[4:5] sc1
	v_pk_mul_f32 v[228:229], v[64:65], v[248:249] op_sel:[0,0] op_sel_hi:[1,0]
	v_pk_mul_f32 v[230:231], v[66:67], v[248:249] op_sel:[0,0] op_sel_hi:[1,0]
	v_pk_mul_f32 v[232:233], v[60:61], v[248:249] op_sel:[0,0] op_sel_hi:[1,0]
	v_pk_mul_f32 v[234:235], v[62:63], v[248:249] op_sel:[0,0] op_sel_hi:[1,0]
	v_exp_f32_e32 v228, v228
	v_exp_f32_e32 v229, v229
	v_exp_f32_e32 v230, v230
	v_exp_f32_e32 v231, v231
	v_exp_f32_e32 v232, v232
	v_exp_f32_e32 v233, v233
	v_exp_f32_e32 v234, v234
	v_exp_f32_e32 v235, v235
	v_pk_fma_f32 v[228:229], v[228:229], v[240:241], v[240:241] op_sel:[0,0,0] op_sel_hi:[1,0,0]
	v_pk_fma_f32 v[230:231], v[230:231], v[240:241], v[240:241] op_sel:[0,0,0] op_sel_hi:[1,0,0]
	v_pk_fma_f32 v[232:233], v[232:233], v[240:241], v[240:241] op_sel:[0,0,0] op_sel_hi:[1,0,0]
	v_pk_fma_f32 v[234:235], v[234:235], v[240:241], v[240:241] op_sel:[0,0,0] op_sel_hi:[1,0,0]
	v_rcp_f32_e32 v228, v228
	v_rcp_f32_e32 v229, v229
	v_rcp_f32_e32 v230, v230
	v_rcp_f32_e32 v231, v231
	v_rcp_f32_e32 v232, v232
	v_rcp_f32_e32 v233, v233
	v_rcp_f32_e32 v234, v234
	v_rcp_f32_e32 v235, v235
	v_pk_mul_f32 v[56:57], v[64:65], v[56:57]
	v_pk_mul_f32 v[58:59], v[66:67], v[58:59]
	v_pk_mul_f32 v[52:53], v[60:61], v[52:53]
	v_pk_mul_f32 v[54:55], v[62:63], v[54:55]
	v_add_u32_e32 v252, 0x6e000, v252
	v_pk_mul_f32 v[64:65], v[56:57], v[228:229]
	v_pk_mul_f32 v[66:67], v[58:59], v[230:231]
	v_pk_mul_f32 v[60:61], v[52:53], v[232:233]
	v_pk_mul_f32 v[62:63], v[54:55], v[234:235]
	v_cvt_pk_bf16_f32 v64, v64, v65
	v_cvt_pk_bf16_f32 v65, v66, v67
	v_cvt_pk_bf16_f32 v66, v60, v61
	v_cvt_pk_bf16_f32 v67, v62, v63
	global_store_dwordx4 v252, v[64:67], s[4:5] sc1
	v_pk_mul_f32 v[228:229], v[48:49], v[248:249] op_sel:[0,1] op_sel_hi:[1,1]
	v_pk_mul_f32 v[230:231], v[50:51], v[248:249] op_sel:[0,1] op_sel_hi:[1,1]
	v_pk_mul_f32 v[232:233], v[44:45], v[248:249] op_sel:[0,1] op_sel_hi:[1,1]
	v_pk_mul_f32 v[234:235], v[46:47], v[248:249] op_sel:[0,1] op_sel_hi:[1,1]
	v_exp_f32_e32 v228, v228
	v_exp_f32_e32 v229, v229
	v_exp_f32_e32 v230, v230
	v_exp_f32_e32 v231, v231
	v_exp_f32_e32 v232, v232
	v_exp_f32_e32 v233, v233
	v_exp_f32_e32 v234, v234
	v_exp_f32_e32 v235, v235
	v_pk_fma_f32 v[228:229], v[228:229], v[240:241], v[240:241] op_sel:[0,1,1] op_sel_hi:[1,1,1]
; __device__ __forceinline__ float sigm(float x) { return __builtin_amdgcn_rcpf(1.0f + __builtin_amdgcn_exp2f(-1.4426950408889634f * x)); }
; __device__ __forceinline__ u32x4 pack8(const f32x4 a, const f32x4 b) { u32x4 w; w.x = cvt_pk_bf16(a[0], a[1]); w.y = cvt_pk_bf16(a[2], a[3]); w.z = cvt_pk_bf16(b[0], b[1]); w.w = cvt_pk_bf16(b[2], b[3]); return w; }
;     __device__ __forceinline__ void operator()(const f32x4 (&acc)[2][2][4][2], const Unit& u, int wr, int wc, int fr, int fq) const {
;     ...
;         for (int ai = 0; ai < 2; ++ai) { if (ai == 1 && u.half != 0) break;
; #pragma unroll
;             for (int m = 0; m < 4; ++m) { const float rf = rsr[ai * HALF + m * 16]; f32x4 v0 = acc[ai][0][m][0] * rf, v1 = acc[ai][0][m][1] * rf; const f32x4 u0 = acc[ai][1][m][0] * rf, u1 = acc[ai][1][m][1] * rf;
; #pragma unroll
;                 for (int e = 0; e < 4; ++e) { v0[e] = v0[e] * sigm(v0[e]) * u0[e]; v1[e] = v1[e] * sigm(v1[e]) * u1[e]; }
;                 *(u32x4*)(H + (size_t)(row0 + ai * HALF + m * 16) * DFF + col0) = pack8(v0, v1); } }
	v_pk_fma_f32 v[230:231], v[230:231], v[240:241], v[240:241] op_sel:[0,1,1] op_sel_hi:[1,1,1]
	v_pk_fma_f32 v[232:233], v[232:233], v[240:241], v[240:241] op_sel:[0,1,1] op_sel_hi:[1,1,1]
	v_pk_fma_f32 v[234:235], v[234:235], v[240:241], v[240:241] op_sel:[0,1,1] op_sel_hi:[1,1,1]
	v_rcp_f32_e32 v228, v228
	v_rcp_f32_e32 v229, v229
	v_rcp_f32_e32 v230, v230
	v_rcp_f32_e32 v231, v231
	v_rcp_f32_e32 v232, v232
	v_rcp_f32_e32 v233, v233
	v_rcp_f32_e32 v234, v234
	v_rcp_f32_e32 v235, v235
	v_pk_mul_f32 v[40:41], v[48:49], v[40:41]
	v_pk_mul_f32 v[42:43], v[50:51], v[42:43]
	v_pk_mul_f32 v[36:37], v[44:45], v[36:37]
	v_pk_mul_f32 v[38:39], v[46:47], v[38:39]
	v_add_u32_e32 v252, 0x16000, v252
	v_pk_mul_f32 v[48:49], v[40:41], v[228:229]
	v_pk_mul_f32 v[50:51], v[42:43], v[230:231]
	v_pk_mul_f32 v[44:45], v[36:37], v[232:233]
	v_pk_mul_f32 v[46:47], v[38:39], v[234:235]
	v_cvt_pk_bf16_f32 v40, v48, v49
	v_cvt_pk_bf16_f32 v41, v50, v51
	v_cvt_pk_bf16_f32 v42, v44, v45
	v_cvt_pk_bf16_f32 v43, v46, v47
	global_store_dwordx4 v252, v[40:43], s[4:5] sc1
	v_pk_mul_f32 v[228:229], v[32:33], v[250:251] op_sel:[0,0] op_sel_hi:[1,0]
	v_pk_mul_f32 v[230:231], v[34:35], v[250:251] op_sel:[0,0] op_sel_hi:[1,0]
	v_pk_mul_f32 v[232:233], v[28:29], v[250:251] op_sel:[0,0] op_sel_hi:[1,0]
	v_pk_mul_f32 v[234:235], v[30:31], v[250:251] op_sel:[0,0] op_sel_hi:[1,0]
	v_exp_f32_e32 v228, v228
	v_exp_f32_e32 v229, v229
	v_exp_f32_e32 v230, v230
	v_exp_f32_e32 v231, v231
	v_exp_f32_e32 v232, v232
	v_exp_f32_e32 v233, v233
	v_exp_f32_e32 v234, v234
	v_exp_f32_e32 v235, v235
	v_pk_fma_f32 v[228:229], v[228:229], v[242:243], v[242:243] op_sel:[0,0,0] op_sel_hi:[1,0,0]
	v_pk_fma_f32 v[230:231], v[230:231], v[242:243], v[242:243] op_sel:[0,0,0] op_sel_hi:[1,0,0]
	v_pk_fma_f32 v[232:233], v[232:233], v[242:243], v[242:243] op_sel:[0,0,0] op_sel_hi:[1,0,0]
	v_pk_fma_f32 v[234:235], v[234:235], v[242:243], v[242:243] op_sel:[0,0,0] op_sel_hi:[1,0,0]
	v_rcp_f32_e32 v228, v228
	v_rcp_f32_e32 v229, v229
	v_rcp_f32_e32 v230, v230
	v_rcp_f32_e32 v231, v231
	v_rcp_f32_e32 v232, v232
	v_rcp_f32_e32 v233, v233
	v_rcp_f32_e32 v234, v234
	v_rcp_f32_e32 v235, v235
	v_pk_mul_f32 v[24:25], v[32:33], v[24:25]
	v_pk_mul_f32 v[26:27], v[34:35], v[26:27]
	v_pk_mul_f32 v[20:21], v[28:29], v[20:21]
	v_pk_mul_f32 v[22:23], v[30:31], v[22:23]
	v_add_u32_e32 v252, 0x16000, v252
	v_pk_mul_f32 v[32:33], v[24:25], v[228:229]
	v_pk_mul_f32 v[34:35], v[26:27], v[230:231]
	v_pk_mul_f32 v[28:29], v[20:21], v[232:233]
	v_pk_mul_f32 v[30:31], v[22:23], v[234:235]
	v_cvt_pk_bf16_f32 v32, v32, v33
	v_cvt_pk_bf16_f32 v33, v34, v35
	v_cvt_pk_bf16_f32 v34, v28, v29
	v_cvt_pk_bf16_f32 v35, v30, v31
	global_store_dwordx4 v252, v[32:35], s[4:5] sc1
	v_pk_mul_f32 v[228:229], v[16:17], v[250:251] op_sel:[0,1] op_sel_hi:[1,1]
	v_pk_mul_f32 v[230:231], v[18:19], v[250:251] op_sel:[0,1] op_sel_hi:[1,1]
	v_pk_mul_f32 v[232:233], v[12:13], v[250:251] op_sel:[0,1] op_sel_hi:[1,1]
	v_pk_mul_f32 v[234:235], v[14:15], v[250:251] op_sel:[0,1] op_sel_hi:[1,1]
	v_exp_f32_e32 v228, v228
	v_exp_f32_e32 v229, v229
	v_exp_f32_e32 v230, v230
	v_exp_f32_e32 v231, v231
	v_exp_f32_e32 v232, v232
	v_exp_f32_e32 v233, v233
	v_exp_f32_e32 v234, v234
	v_exp_f32_e32 v235, v235
	v_pk_fma_f32 v[228:229], v[228:229], v[242:243], v[242:243] op_sel:[0,1,1] op_sel_hi:[1,1,1]
	v_pk_fma_f32 v[230:231], v[230:231], v[242:243], v[242:243] op_sel:[0,1,1] op_sel_hi:[1,1,1]
	v_pk_fma_f32 v[232:233], v[232:233], v[242:243], v[242:243] op_sel:[0,1,1] op_sel_hi:[1,1,1]
	v_pk_fma_f32 v[234:235], v[234:235], v[242:243], v[242:243] op_sel:[0,1,1] op_sel_hi:[1,1,1]
	v_rcp_f32_e32 v228, v228
	v_rcp_f32_e32 v229, v229
	v_rcp_f32_e32 v230, v230
	v_rcp_f32_e32 v231, v231
	v_rcp_f32_e32 v232, v232
	v_rcp_f32_e32 v233, v233
	v_rcp_f32_e32 v234, v234
	v_rcp_f32_e32 v235, v235
	v_pk_mul_f32 v[8:9], v[16:17], v[8:9]
	v_pk_mul_f32 v[10:11], v[18:19], v[10:11]
	v_pk_mul_f32 v[4:5], v[12:13], v[4:5]
	v_pk_mul_f32 v[6:7], v[14:15], v[6:7]
	v_add_u32_e32 v252, 0x16000, v252
	v_pk_mul_f32 v[16:17], v[8:9], v[228:229]
	v_pk_mul_f32 v[18:19], v[10:11], v[230:231]
	v_pk_mul_f32 v[12:13], v[4:5], v[232:233]
	v_pk_mul_f32 v[14:15], v[6:7], v[234:235]
	v_cvt_pk_bf16_f32 v8, v16, v17
	v_cvt_pk_bf16_f32 v9, v18, v19
	v_cvt_pk_bf16_f32 v10, v12, v13
	v_cvt_pk_bf16_f32 v11, v14, v15
	global_store_dwordx4 v252, v[8:11], s[4:5] sc1
	s_andn2_b64 vcc, exec, s[38:39]
	s_mov_b64 s[0:1], -1
	s_cbranch_vccnz .LBB0_1473
	s_andn2_b64 vcc, exec, s[8:9]
	s_cbranch_vccnz .LBB0_1472
	s_barrier
	s_branch .LBB0_1472
